# P2 in-projection GEMM: unit groups of 4 row tiles (was 2): fewer distinct A/B panels per XCD round, better L2 reuse beside the weight-conversion stream
# speedup vs baseline: 1.0110x; 1.0097x over previous
.LBB0_267:
	s_cmpk_gt_i32 s20, 0x6ff
	v_readfirstlane_b32 s10, v0
	s_cbranch_scc1 .LBB0_289
	s_add_u32 s16, s76, 0x8687b000
	s_addc_u32 s17, s77, 0
	s_add_u32 s18, s76, 0x6c00
	s_addc_u32 s19, s77, 0
	s_ashr_i32 s21, s20, 31
	s_lshr_b32 s0, s21, 29
	s_add_i32 s0, s20, s0
	s_ashr_i32 s1, s0, 3
	s_and_b32 s0, s0, -8
	s_sub_i32 s0, s20, s0
	s_cmp_lt_i32 s0, 0
	s_movk_i32 s4, 0xe1
	s_cselect_b32 s4, s4, 0xe0
	s_mul_i32 s0, s0, s4
	s_add_i32 s0, s0, s1
	s_mul_hi_i32 s1, s0, 0x92492493
	s_add_i32 s1, s1, s0
	s_lshr_b32 s4, s1, 31
	s_ashr_i32 s1, s1, 6
	s_add_i32 s4, s1, s4
	s_lshl_b32 s1, s4, 2
	s_mul_i32 s4, s4, 112
	s_sub_i32 s0, s0, s4
	s_bfe_u32 s4, s0, 0x10007
	s_add_i32 s4, s0, s4
	s_bfe_i32 s6, s4, 0x80000
	s_sext_i32_i16 s12, s6
	s_and_b32 s4, s4, 0xfc
	s_sub_i32 s0, s0, s4
	s_ashr_i32 s74, s12, 2
	s_cmpk_lt_u32 s10, 0x100
	s_sext_i32_i8 s11, s0
	s_cselect_b64 s[6:7], -1, 0
	s_and_b32 s0, s10, 0xffffffc0
	s_mov_b32 s5, 0
	s_cmpk_gt_u32 s10, 0xff
	s_mov_b64 s[8:9], -1
	s_cbranch_scc0 .LBB0_270
	s_lshl_b32 s8, s74, 8
	s_ashr_i32 s9, s8, 31
	s_lshl_b64 s[8:9], s[8:9], 2
	s_add_u32 s13, s18, s8
	s_addc_u32 s14, s19, s9
	s_add_i32 s4, s0, 0xffffff00
	s_lshl_b64 s[8:9], s[4:5], 2
	s_add_u32 s8, s13, s8
	s_addc_u32 s9, s14, s9
	s_lshl_b32 s4, s4, 2
	s_add_i32 s4, s4, 0
	s_waitcnt vmcnt(6)
	v_lshlrev_b32_e32 v2, 2, v190
	s_add_i32 m0, s4, 0x20800
	s_nop 0
	global_load_lds_dword v2, s[8:9]
	s_mov_b64 s[8:9], 0
.LBB0_270:
	s_lshr_b32 s4, s12, 2
	s_andn2_b64 vcc, exec, s[8:9]
	s_waitcnt lgkmcnt(0)
	s_add_i32 s42, s1, s11
	s_cbranch_vccnz .LBB0_272
	s_lshl_b32 s8, s42, 8
	s_ashr_i32 s9, s8, 31
	s_lshl_b64 s[8:9], s[8:9], 2
	s_add_u32 s5, s16, s8
	s_mov_b32 s1, 0
	s_addc_u32 s11, s17, s9
	s_lshl_b64 s[8:9], s[0:1], 2
	s_add_u32 s8, s5, s8
	s_addc_u32 s9, s11, s9
	s_lshl_b32 s1, s0, 2
	s_add_i32 s1, s1, 0
	s_waitcnt vmcnt(0)
	v_lshlrev_b32_e32 v2, 2, v190
	s_add_i32 m0, s1, 0x22000
	s_nop 0
	global_load_lds_dword v2, s[8:9]

.LBB0_277:
	s_add_i32 s73, s15, 1
	s_mul_i32 s0, s73, s67
	s_mul_hi_u32 s1, s73, s24
	s_add_i32 s1, s1, s0
	s_mul_i32 s0, s73, s24
	s_add_u32 s4, s0, s20
	s_addc_u32 s5, s1, s21
	v_cmp_gt_i64_e32 vcc, s[4:5], v[150:151]
	v_cmp_lt_i64_e64 s[0:1], s[4:5], v[148:149]
	s_cbranch_vccnz .LBB0_279
	s_ashr_i32 s5, s4, 31
	s_lshr_b32 s5, s5, 29
	s_add_i32 s5, s4, s5
	s_ashr_i32 s16, s5, 3
	s_and_b32 s5, s5, -8
	s_sub_i32 s4, s4, s5
	s_cmp_lt_i32 s4, 0
	s_cselect_b32 s5, s69, 0xe0
	s_mul_i32 s4, s4, s5
	s_add_i32 s4, s4, s16
	s_mul_hi_i32 s5, s4, 0x92492493
	s_add_i32 s5, s5, s4
	s_lshr_b32 s16, s5, 31
	s_ashr_i32 s5, s5, 6
	s_add_i32 s5, s5, s16
	s_lshl_b32 s17, s5, 2
	s_sub_i32 s16, 64, s17
	s_min_i32 s18, s16, 4
	s_abs_i32 s16, s18
	v_cvt_f32_u32_e32 v2, s16
	s_sub_i32 s22, 0, s16
	s_mul_i32 s5, s5, 112
	s_sub_i32 s4, s4, s5
	v_rcp_iflag_f32_e32 v2, v2
	s_abs_i32 s5, s4
	s_xor_b32 s19, s4, s18
	s_ashr_i32 s19, s19, 31
	v_mul_f32_e32 v2, 0x4f7ffffe, v2
	v_cvt_u32_f32_e32 v2, v2
	s_nop 0
	v_readfirstlane_b32 s23, v2
	s_mul_i32 s22, s22, s23
	s_mul_hi_u32 s22, s23, s22
	s_add_i32 s23, s23, s22
	s_mul_hi_u32 s22, s5, s23
	s_mul_i32 s23, s22, s16
	s_sub_i32 s5, s5, s23
	s_add_i32 s56, s22, 1
	s_sub_i32 s23, s5, s16
	s_cmp_ge_u32 s5, s16
	s_cselect_b32 s22, s56, s22
	s_cselect_b32 s5, s23, s5
	s_add_i32 s23, s22, 1
	s_cmp_ge_u32 s5, s16
	s_cselect_b32 s5, s23, s22
	s_xor_b32 s5, s5, s19
	s_sub_i32 s16, s5, s19
	s_mul_i32 s5, s16, s18
	s_sub_i32 s4, s4, s5
	s_add_i32 s18, s17, s4
